# P2 epilogue writes full 128-B lines (W_in rows permuted at conversion, DPP lane exchange) + mLSTM LDS read batching
# speedup vs baseline: 1.0109x; 1.0013x over previous
.LBB0_67:
	v_mov_b32_e32 v3, s16
	ds_read_b64 v[22:23], v3
	s_mul_hi_i32 s0, s8, 0x2aaaaaab
	s_lshr_b32 s2, s0, 31
	s_ashr_i32 s0, s0, 5
	s_add_i32 s0, s0, s2
	s_waitcnt lgkmcnt(0)
	v_readfirstlane_b32 s3, v22
	s_mul_i32 s2, s0, 0xc0
	v_readfirstlane_b32 s4, v23
	v_mov_b32_e32 v22, s3
	s_sub_i32 s3, s8, s2
	s_lshl_b32 s2, s0, 6
	s_lshl_b32 s0, s3, 5
	s_and_b32 s100, s0, 0xffffff00
	s_bfe_u32 s101, s0, 0x10005
	s_lshl_b32 s101, s101, 7
	s_or_b32 s100, s100, s101
	s_bfe_u32 s101, s0, 0x20006
	s_lshl_b32 s101, s101, 5
	s_or_b32 s100, s100, s101
	v_or_b32_e32 v30, s0, v25
	v_mov_b32_e32 v23, s4
	v_ashrrev_i32_e32 v31, 31, v30
	v_cmp_gt_i32_e32 vcc, s17, v30
	v_lshl_add_u64 v[22:23], v[30:31], 2, v[22:23]
	s_mov_b32 s3, 0
	v_cndmask_b32_e64 v6, 64, 0, vcc
	v_lshl_add_u64 v[22:23], v[22:23], 0, v[6:7]
	v_or_b32_e32 v3, s2, v1
	v_or_b32_e32 v6, s2, v2
	s_mov_b32 s4, 1
	s_mov_b32 s5, 32
.LBB0_68:
	s_lshl_b32 s19, s4, 1
	s_lshl_b32 s22, s3, 1
	v_or_b32_e32 v24, s19, v3
	v_or_b32_e32 v30, s22, v6
	s_add_i32 s23, s19, 4
	s_add_i32 s24, s22, 4
	s_add_i32 s25, s19, 8
	s_add_i32 s26, s22, 8
	s_add_i32 s27, s19, 12
	s_add_i32 s28, s22, 12
	s_add_i32 s29, s19, 16
	s_add_i32 s30, s22, 16
	s_add_i32 s31, s19, 20
	s_add_i32 s33, s22, 20
	s_add_i32 s34, s19, 24
	s_add_i32 s35, s22, 24
	s_add_i32 s36, s19, 28
	s_add_i32 s37, s22, 28
	v_mad_i64_i32 v[30:31], s[20:21], v30, s18, v[22:23]
	v_mad_i64_i32 v[32:33], s[20:21], v24, s18, v[22:23]
	v_or_b32_e32 v24, s23, v3
	v_or_b32_e32 v34, s24, v6
	v_or_b32_e32 v40, s25, v3
	v_or_b32_e32 v38, s26, v6
	v_or_b32_e32 v44, s27, v3
	v_or_b32_e32 v42, s28, v6
	v_or_b32_e32 v48, s29, v3
	v_or_b32_e32 v46, s30, v6
	v_or_b32_e32 v52, s31, v3
	v_or_b32_e32 v50, s33, v6
	v_or_b32_e32 v56, s34, v3
	v_or_b32_e32 v54, s35, v6
	v_or_b32_e32 v60, s36, v3
	v_or_b32_e32 v58, s37, v6
	v_mad_i64_i32 v[34:35], s[20:21], v34, s18, v[22:23]
	v_mad_i64_i32 v[36:37], s[20:21], v24, s18, v[22:23]
	v_mad_i64_i32 v[38:39], s[20:21], v38, s18, v[22:23]
	v_mad_i64_i32 v[40:41], s[20:21], v40, s18, v[22:23]
	v_mad_i64_i32 v[42:43], s[20:21], v42, s18, v[22:23]
	v_mad_i64_i32 v[44:45], s[20:21], v44, s18, v[22:23]
	v_mad_i64_i32 v[46:47], s[20:21], v46, s18, v[22:23]
	v_mad_i64_i32 v[48:49], s[20:21], v48, s18, v[22:23]
	v_mad_i64_i32 v[50:51], s[20:21], v50, s18, v[22:23]
	v_mad_i64_i32 v[52:53], s[20:21], v52, s18, v[22:23]
	v_mad_i64_i32 v[54:55], s[20:21], v54, s18, v[22:23]
	v_mad_i64_i32 v[56:57], s[20:21], v56, s18, v[22:23]
	v_mad_i64_i32 v[58:59], s[20:21], v58, s18, v[22:23]
	v_mad_i64_i32 v[60:61], s[20:21], v60, s18, v[22:23]
	global_load_dword v24, v[30:31], off
	global_load_dword v62, v[32:33], off
	global_load_dword v63, v[34:35], off
	global_load_dword v64, v[36:37], off
	global_load_dword v65, v[38:39], off
	global_load_dword v66, v[40:41], off
	global_load_dword v67, v[42:43], off
	global_load_dword v68, v[44:45], off
	global_load_dword v69, v[46:47], off
	global_load_dword v70, v[48:49], off
	global_load_dword v71, v[50:51], off
	global_load_dword v72, v[52:53], off
	global_load_dword v73, v[54:55], off
	global_load_dword v74, v[56:57], off
	global_load_dword v75, v[58:59], off
	global_load_dword v76, v[60:61], off
	v_or_b32_e32 v32, s19, v1
	v_or_b32_e32 v30, s22, v2
	s_add_i32 s3, s3, 16
	s_add_i32 s4, s4, 16
	s_add_i32 s5, s5, -16
	v_mad_u64_u32 v[30:31], s[20:21], v30, s10, v[4:5]
	v_mad_u64_u32 v[32:33], s[20:21], v32, s10, v[4:5]
	v_or_b32_e32 v31, s23, v1
	v_or_b32_e32 v33, s24, v2
	v_or_b32_e32 v40, s25, v1
	v_or_b32_e32 v38, s26, v2
	v_or_b32_e32 v44, s27, v1
	v_or_b32_e32 v42, s28, v2
	v_or_b32_e32 v48, s29, v1
	v_or_b32_e32 v46, s30, v2
	v_or_b32_e32 v52, s31, v1
	v_or_b32_e32 v50, s33, v2
	v_or_b32_e32 v56, s34, v1
	v_or_b32_e32 v54, s35, v2
	v_or_b32_e32 v60, s36, v1
	v_or_b32_e32 v58, s37, v2
	s_cmp_lg_u32 s5, 0
	v_mad_u64_u32 v[34:35], s[20:21], v33, s10, v[4:5]
	v_mad_u64_u32 v[36:37], s[20:21], v31, s10, v[4:5]
	v_mad_u64_u32 v[38:39], s[20:21], v38, s10, v[4:5]
	v_mad_u64_u32 v[40:41], s[20:21], v40, s10, v[4:5]
	v_mad_u64_u32 v[42:43], s[20:21], v42, s10, v[4:5]
	v_mad_u64_u32 v[44:45], s[20:21], v44, s10, v[4:5]
	v_mad_u64_u32 v[46:47], s[20:21], v46, s10, v[4:5]
	v_mad_u64_u32 v[48:49], s[20:21], v48, s10, v[4:5]
	v_mad_u64_u32 v[50:51], s[20:21], v50, s10, v[4:5]
	v_mad_u64_u32 v[52:53], s[20:21], v52, s10, v[4:5]
	v_mad_u64_u32 v[54:55], s[20:21], v54, s10, v[4:5]
	v_mad_u64_u32 v[56:57], s[20:21], v56, s10, v[4:5]
	v_mad_u64_u32 v[58:59], s[20:21], v58, s10, v[4:5]
	v_mad_u64_u32 v[60:61], s[20:21], v60, s10, v[4:5]
	s_waitcnt vmcnt(15)
	ds_write_b32 v30, v24
	s_waitcnt vmcnt(14)
	ds_write_b32 v32, v62
	s_waitcnt vmcnt(13)
	ds_write_b32 v34, v63
	s_waitcnt vmcnt(12)
	ds_write_b32 v36, v64
	s_waitcnt vmcnt(11)
	ds_write_b32 v38, v65
	s_waitcnt vmcnt(10)
	ds_write_b32 v40, v66
	s_waitcnt vmcnt(9)
	ds_write_b32 v42, v67
	s_waitcnt vmcnt(8)
	ds_write_b32 v44, v68
	s_waitcnt vmcnt(7)
	ds_write_b32 v46, v69
	s_waitcnt vmcnt(6)
	ds_write_b32 v48, v70
	s_waitcnt vmcnt(5)
	ds_write_b32 v50, v71
	s_waitcnt vmcnt(4)
	ds_write_b32 v52, v72
	s_waitcnt vmcnt(3)
	ds_write_b32 v54, v73
	s_waitcnt vmcnt(2)
	ds_write_b32 v56, v74
	s_waitcnt vmcnt(1)
	ds_write_b32 v58, v75
	s_waitcnt vmcnt(0)
	ds_write_b32 v60, v76
	s_cbranch_scc1 .LBB0_68
	s_waitcnt lgkmcnt(0)
	ds_read2_b32 v[22:23], v26 offset0:33 offset1:41
	ds_read2_b32 v[34:35], v26 offset0:66 offset1:74
	ds_read2_b32 v[36:37], v26 offset0:132 offset1:140
	ds_read2_b32 v[38:39], v26 offset0:198 offset1:206
	ds_read2_b32 v[40:41], v26 offset0:231 offset1:239
	ds_read2_b32 v[42:43], v26 offset0:165 offset1:173
	ds_read2_b32 v[44:45], v26 offset0:99 offset1:107
	ds_read2_b32 v[46:47], v26 offset1:8
	v_or_b32_e32 v50, s100, v5
	s_ashr_i32 s3, s2, 31
	v_ashrrev_i32_e32 v51, 31, v50
	v_lshl_add_u64 v[48:49], s[2:3], 1, v[16:17]
	v_lshlrev_b64 v[50:51], 11, v[50:51]
	s_waitcnt lgkmcnt(3)
	v_cvt_pk_f16_f32 v33, v38, v40
	s_waitcnt lgkmcnt(2)
	v_cvt_pk_f16_f32 v32, v36, v42
	s_waitcnt lgkmcnt(1)
	v_cvt_pk_f16_f32 v31, v34, v44
	s_waitcnt lgkmcnt(0)
	v_cvt_pk_f16_f32 v30, v46, v22
	v_lshl_add_u64 v[50:51], v[48:49], 0, v[50:51]
	v_or_b32_e32 v22, s100, v27
	global_store_dwordx4 v[50:51], v[30:33], off
	s_nop 1
	v_cvt_pk_f16_f32 v30, v47, v23
	v_ashrrev_i32_e32 v23, 31, v22
	v_cvt_pk_f16_f32 v33, v39, v41
	v_cvt_pk_f16_f32 v32, v37, v43
	v_cvt_pk_f16_f32 v31, v35, v45
	v_lshlrev_b64 v[22:23], 11, v[22:23]
	ds_read2_b32 v[34:35], v26 offset0:49 offset1:57
	ds_read2_b32 v[36:37], v26 offset0:82 offset1:90
	ds_read2_b32 v[38:39], v26 offset0:148 offset1:156
	ds_read2_b32 v[40:41], v26 offset0:214 offset1:222
	ds_read2_b32 v[42:43], v26 offset0:247 offset1:255
	ds_read2_b32 v[44:45], v26 offset0:181 offset1:189
	ds_read2_b32 v[46:47], v26 offset0:115 offset1:123
	ds_read2_b32 v[50:51], v26 offset0:16 offset1:24
	v_lshl_add_u64 v[22:23], v[48:49], 0, v[22:23]
	global_store_dwordx4 v[22:23], v[30:33], off
	v_or_b32_e32 v22, s100, v28
	v_ashrrev_i32_e32 v23, 31, v22
	v_lshlrev_b64 v[22:23], 11, v[22:23]
	s_waitcnt lgkmcnt(3)
	v_cvt_pk_f16_f32 v33, v40, v42
	s_waitcnt lgkmcnt(2)
	v_cvt_pk_f16_f32 v32, v38, v44
	s_waitcnt lgkmcnt(1)
	v_cvt_pk_f16_f32 v31, v36, v46
	s_waitcnt lgkmcnt(0)
	v_cvt_pk_f16_f32 v30, v50, v34
	v_lshl_add_u64 v[22:23], v[48:49], 0, v[22:23]
	global_store_dwordx4 v[22:23], v[30:33], off
	v_or_b32_e32 v22, s100, v29
	v_ashrrev_i32_e32 v23, 31, v22
	v_lshlrev_b64 v[22:23], 11, v[22:23]
	v_cvt_pk_f16_f32 v33, v41, v43
	v_cvt_pk_f16_f32 v32, v39, v45
	v_cvt_pk_f16_f32 v31, v37, v47
	v_cvt_pk_f16_f32 v30, v51, v35
	v_lshl_add_u64 v[22:23], v[48:49], 0, v[22:23]
	global_store_dwordx4 v[22:23], v[30:33], off
	s_waitcnt lgkmcnt(0)
	s_branch .LBB0_31

.LBB0_214:
	s_cmp_lt_i32 s1, 0
	s_cbranch_scc0 .Lp2e0_done
	v_and_b32_e32 v162, 8, v1
	v_sub_u32_e32 v163, v1, v162
	v_lshl_add_u32 v163, s4, 8, v163
	v_and_b32_e32 v164, 0x60, v156
	v_and_b32_e32 v165, 24, v156
	v_lshl_add_u32 v164, v164, 1, v165
	v_lshl_or_b32 v164, s0, 8, v164
	v_lshlrev_b32_e32 v165, 2, v162
	v_add_u32_e32 v166, v164, v165
	v_xor_b32_e32 v165, 32, v165
	v_add_u32_e32 v167, v164, v165
	v_mov_b64_e32 v[168:169], s[6:7]
	v_mad_i64_i32 v[168:169], s[22:23], v163, s49, v[168:169]
	v_mov_b32_e32 v171, 0
	v_lshlrev_b32_e32 v170, 1, v166
	v_lshl_add_u64 v[172:173], v[168:169], 0, v[170:171]
	v_lshlrev_b32_e32 v170, 1, v167
	v_add_u32_e32 v170, 0x18000, v170
	v_lshl_add_u64 v[174:175], v[168:169], 0, v[170:171]
	v_cmp_ne_u32_e64 s[22:23], 0, v162
	v_mov_b32_e32 v178, 0x30000
	v_mov_b32_e32 v179, 0
	v_mov_b32_e32 v200, 0xf0000
	v_mov_b32_e32 v201, 0
	s_cmp_eq_u32 s0, 1
	s_cselect_b32 s4, 0x3e000000, 1.0
	v_mov_b32_e32 v176, s4
	s_cmp_gt_u32 s0, 9
	s_cbranch_scc1 .Lp2e0_sig
	v_mul_f32_e32 v126, v176, v126
	v_mul_f32_e32 v127, v176, v127
	v_mul_f32_e32 v128, v176, v128
	v_mul_f32_e32 v129, v176, v129
	v_mul_f32_e32 v122, v176, v122
	v_mul_f32_e32 v123, v176, v123
	v_mul_f32_e32 v124, v176, v124
	v_mul_f32_e32 v125, v176, v125
	v_mul_f32_e32 v118, v176, v118
	v_mul_f32_e32 v119, v176, v119
	v_mul_f32_e32 v120, v176, v120
	v_mul_f32_e32 v121, v176, v121
	v_mul_f32_e32 v114, v176, v114
	v_mul_f32_e32 v115, v176, v115
	v_mul_f32_e32 v116, v176, v116
	v_mul_f32_e32 v117, v176, v117
	v_cvt_pk_f16_f32 v184, v118, v119
	v_cvt_pk_f16_f32 v185, v120, v121
	v_cvt_pk_f16_f32 v186, v114, v115
	v_cvt_pk_f16_f32 v187, v116, v117
	v_cvt_pk_f16_f32 v180, v126, v127
	v_cvt_pk_f16_f32 v181, v128, v129
	v_cvt_pk_f16_f32 v182, v122, v123
	v_cvt_pk_f16_f32 v183, v124, v125
	v_mov_b32_dpp v188, v184 row_ror:8 row_mask:0xf bank_mask:0xf
	v_mov_b32_dpp v189, v185 row_ror:8 row_mask:0xf bank_mask:0xf
	v_mov_b32_dpp v190, v186 row_ror:8 row_mask:0xf bank_mask:0xf
	v_mov_b32_dpp v191, v187 row_ror:8 row_mask:0xf bank_mask:0xf
	v_cndmask_b32_e64 v192, v180, v188, s[22:23]
	v_cndmask_b32_e64 v193, v181, v189, s[22:23]
	v_cndmask_b32_e64 v194, v182, v190, s[22:23]
	v_cndmask_b32_e64 v195, v183, v191, s[22:23]
	v_cndmask_b32_e64 v196, v188, v180, s[22:23]
	v_cndmask_b32_e64 v197, v189, v181, s[22:23]
	v_cndmask_b32_e64 v198, v190, v182, s[22:23]
	v_cndmask_b32_e64 v199, v191, v183, s[22:23]
	global_store_dwordx4 v[172:173], v[192:195], off
	global_store_dwordx4 v[174:175], v[196:199], off
	v_lshl_add_u64 v[172:173], v[172:173], 0, v[178:179]
	v_lshl_add_u64 v[174:175], v[174:175], 0, v[178:179]
	v_mul_f32_e32 v110, v176, v110
	v_mul_f32_e32 v111, v176, v111
	v_mul_f32_e32 v112, v176, v112
	v_mul_f32_e32 v113, v176, v113
	v_mul_f32_e32 v106, v176, v106
	v_mul_f32_e32 v107, v176, v107
	v_mul_f32_e32 v108, v176, v108
	v_mul_f32_e32 v109, v176, v109
	v_mul_f32_e32 v102, v176, v102
	v_mul_f32_e32 v103, v176, v103
	v_mul_f32_e32 v104, v176, v104
	v_mul_f32_e32 v105, v176, v105
	v_mul_f32_e32 v98, v176, v98
	v_mul_f32_e32 v99, v176, v99
	v_mul_f32_e32 v100, v176, v100
	v_mul_f32_e32 v101, v176, v101
	v_cvt_pk_f16_f32 v184, v102, v103
	v_cvt_pk_f16_f32 v185, v104, v105
	v_cvt_pk_f16_f32 v186, v98, v99
	v_cvt_pk_f16_f32 v187, v100, v101
	v_cvt_pk_f16_f32 v180, v110, v111
	v_cvt_pk_f16_f32 v181, v112, v113
	v_cvt_pk_f16_f32 v182, v106, v107
	v_cvt_pk_f16_f32 v183, v108, v109
	v_mov_b32_dpp v188, v184 row_ror:8 row_mask:0xf bank_mask:0xf
	v_mov_b32_dpp v189, v185 row_ror:8 row_mask:0xf bank_mask:0xf
	v_mov_b32_dpp v190, v186 row_ror:8 row_mask:0xf bank_mask:0xf
	v_mov_b32_dpp v191, v187 row_ror:8 row_mask:0xf bank_mask:0xf
	v_cndmask_b32_e64 v192, v180, v188, s[22:23]
	v_cndmask_b32_e64 v193, v181, v189, s[22:23]
	v_cndmask_b32_e64 v194, v182, v190, s[22:23]
	v_cndmask_b32_e64 v195, v183, v191, s[22:23]
	v_cndmask_b32_e64 v196, v188, v180, s[22:23]
	v_cndmask_b32_e64 v197, v189, v181, s[22:23]
	v_cndmask_b32_e64 v198, v190, v182, s[22:23]
	v_cndmask_b32_e64 v199, v191, v183, s[22:23]
	global_store_dwordx4 v[172:173], v[192:195], off
	global_store_dwordx4 v[174:175], v[196:199], off
	v_lshl_add_u64 v[172:173], v[172:173], 0, v[178:179]
	v_lshl_add_u64 v[174:175], v[174:175], 0, v[178:179]
	v_mul_f32_e32 v94, v176, v94
	v_mul_f32_e32 v95, v176, v95
	v_mul_f32_e32 v96, v176, v96
	v_mul_f32_e32 v97, v176, v97
	v_mul_f32_e32 v90, v176, v90
	v_mul_f32_e32 v91, v176, v91
	v_mul_f32_e32 v92, v176, v92
	v_mul_f32_e32 v93, v176, v93
	v_mul_f32_e32 v86, v176, v86
	v_mul_f32_e32 v87, v176, v87
	v_mul_f32_e32 v88, v176, v88
	v_mul_f32_e32 v89, v176, v89
	v_mul_f32_e32 v82, v176, v82
	v_mul_f32_e32 v83, v176, v83
	v_mul_f32_e32 v84, v176, v84
	v_mul_f32_e32 v85, v176, v85
	v_cvt_pk_f16_f32 v184, v86, v87
	v_cvt_pk_f16_f32 v185, v88, v89
	v_cvt_pk_f16_f32 v186, v82, v83
	v_cvt_pk_f16_f32 v187, v84, v85
	v_cvt_pk_f16_f32 v180, v94, v95
	v_cvt_pk_f16_f32 v181, v96, v97
	v_cvt_pk_f16_f32 v182, v90, v91
	v_cvt_pk_f16_f32 v183, v92, v93
	v_mov_b32_dpp v188, v184 row_ror:8 row_mask:0xf bank_mask:0xf
	v_mov_b32_dpp v189, v185 row_ror:8 row_mask:0xf bank_mask:0xf
	v_mov_b32_dpp v190, v186 row_ror:8 row_mask:0xf bank_mask:0xf
	v_mov_b32_dpp v191, v187 row_ror:8 row_mask:0xf bank_mask:0xf
	v_cndmask_b32_e64 v192, v180, v188, s[22:23]
	v_cndmask_b32_e64 v193, v181, v189, s[22:23]
	v_cndmask_b32_e64 v194, v182, v190, s[22:23]
	v_cndmask_b32_e64 v195, v183, v191, s[22:23]
	v_cndmask_b32_e64 v196, v188, v180, s[22:23]
	v_cndmask_b32_e64 v197, v189, v181, s[22:23]
	v_cndmask_b32_e64 v198, v190, v182, s[22:23]
	v_cndmask_b32_e64 v199, v191, v183, s[22:23]
	global_store_dwordx4 v[172:173], v[192:195], off
	global_store_dwordx4 v[174:175], v[196:199], off
	v_lshl_add_u64 v[172:173], v[172:173], 0, v[178:179]
	v_lshl_add_u64 v[174:175], v[174:175], 0, v[178:179]
	v_mul_f32_e32 v78, v176, v78
	v_mul_f32_e32 v79, v176, v79
	v_mul_f32_e32 v80, v176, v80
	v_mul_f32_e32 v81, v176, v81
	v_mul_f32_e32 v74, v176, v74
	v_mul_f32_e32 v75, v176, v75
	v_mul_f32_e32 v76, v176, v76
	v_mul_f32_e32 v77, v176, v77
	v_mul_f32_e32 v70, v176, v70
	v_mul_f32_e32 v71, v176, v71
	v_mul_f32_e32 v72, v176, v72
	v_mul_f32_e32 v73, v176, v73
	v_mul_f32_e32 v66, v176, v66
	v_mul_f32_e32 v67, v176, v67
	v_mul_f32_e32 v68, v176, v68
	v_mul_f32_e32 v69, v176, v69
	v_cvt_pk_f16_f32 v184, v70, v71
	v_cvt_pk_f16_f32 v185, v72, v73
	v_cvt_pk_f16_f32 v186, v66, v67
	v_cvt_pk_f16_f32 v187, v68, v69
	v_cvt_pk_f16_f32 v180, v78, v79
	v_cvt_pk_f16_f32 v181, v80, v81
	v_cvt_pk_f16_f32 v182, v74, v75
	v_cvt_pk_f16_f32 v183, v76, v77
	v_mov_b32_dpp v188, v184 row_ror:8 row_mask:0xf bank_mask:0xf
	v_mov_b32_dpp v189, v185 row_ror:8 row_mask:0xf bank_mask:0xf
	v_mov_b32_dpp v190, v186 row_ror:8 row_mask:0xf bank_mask:0xf
	v_mov_b32_dpp v191, v187 row_ror:8 row_mask:0xf bank_mask:0xf
	v_cndmask_b32_e64 v192, v180, v188, s[22:23]
	v_cndmask_b32_e64 v193, v181, v189, s[22:23]
	v_cndmask_b32_e64 v194, v182, v190, s[22:23]
	v_cndmask_b32_e64 v195, v183, v191, s[22:23]
	v_cndmask_b32_e64 v196, v188, v180, s[22:23]
	v_cndmask_b32_e64 v197, v189, v181, s[22:23]
	v_cndmask_b32_e64 v198, v190, v182, s[22:23]
	v_cndmask_b32_e64 v199, v191, v183, s[22:23]
	global_store_dwordx4 v[172:173], v[192:195], off
	global_store_dwordx4 v[174:175], v[196:199], off
	v_lshl_add_u64 v[172:173], v[172:173], 0, v[200:201]
	v_lshl_add_u64 v[174:175], v[174:175], 0, v[200:201]
	v_mul_f32_e32 v62, v176, v62
	v_mul_f32_e32 v63, v176, v63
	v_mul_f32_e32 v64, v176, v64
	v_mul_f32_e32 v65, v176, v65
	v_mul_f32_e32 v58, v176, v58
	v_mul_f32_e32 v59, v176, v59
	v_mul_f32_e32 v60, v176, v60
	v_mul_f32_e32 v61, v176, v61
	v_mul_f32_e32 v54, v176, v54
	v_mul_f32_e32 v55, v176, v55
	v_mul_f32_e32 v56, v176, v56
	v_mul_f32_e32 v57, v176, v57
	v_mul_f32_e32 v50, v176, v50
	v_mul_f32_e32 v51, v176, v51
	v_mul_f32_e32 v52, v176, v52
	v_mul_f32_e32 v53, v176, v53
	v_cvt_pk_f16_f32 v184, v54, v55
	v_cvt_pk_f16_f32 v185, v56, v57
	v_cvt_pk_f16_f32 v186, v50, v51
	v_cvt_pk_f16_f32 v187, v52, v53
	v_cvt_pk_f16_f32 v180, v62, v63
	v_cvt_pk_f16_f32 v181, v64, v65
	v_cvt_pk_f16_f32 v182, v58, v59
	v_cvt_pk_f16_f32 v183, v60, v61
	v_mov_b32_dpp v188, v184 row_ror:8 row_mask:0xf bank_mask:0xf
	v_mov_b32_dpp v189, v185 row_ror:8 row_mask:0xf bank_mask:0xf
	v_mov_b32_dpp v190, v186 row_ror:8 row_mask:0xf bank_mask:0xf
	v_mov_b32_dpp v191, v187 row_ror:8 row_mask:0xf bank_mask:0xf
	v_cndmask_b32_e64 v192, v180, v188, s[22:23]
	v_cndmask_b32_e64 v193, v181, v189, s[22:23]
	v_cndmask_b32_e64 v194, v182, v190, s[22:23]
	v_cndmask_b32_e64 v195, v183, v191, s[22:23]
	v_cndmask_b32_e64 v196, v188, v180, s[22:23]
	v_cndmask_b32_e64 v197, v189, v181, s[22:23]
	v_cndmask_b32_e64 v198, v190, v182, s[22:23]
	v_cndmask_b32_e64 v199, v191, v183, s[22:23]
	global_store_dwordx4 v[172:173], v[192:195], off
	global_store_dwordx4 v[174:175], v[196:199], off
	v_lshl_add_u64 v[172:173], v[172:173], 0, v[178:179]
	v_lshl_add_u64 v[174:175], v[174:175], 0, v[178:179]
	v_mul_f32_e32 v46, v176, v46
	v_mul_f32_e32 v47, v176, v47
	v_mul_f32_e32 v48, v176, v48
	v_mul_f32_e32 v49, v176, v49
	v_mul_f32_e32 v42, v176, v42
	v_mul_f32_e32 v43, v176, v43
	v_mul_f32_e32 v44, v176, v44
	v_mul_f32_e32 v45, v176, v45
	v_mul_f32_e32 v38, v176, v38
	v_mul_f32_e32 v39, v176, v39
	v_mul_f32_e32 v40, v176, v40
	v_mul_f32_e32 v41, v176, v41
	v_mul_f32_e32 v34, v176, v34
	v_mul_f32_e32 v35, v176, v35
	v_mul_f32_e32 v36, v176, v36
	v_mul_f32_e32 v37, v176, v37
	v_cvt_pk_f16_f32 v184, v38, v39
	v_cvt_pk_f16_f32 v185, v40, v41
	v_cvt_pk_f16_f32 v186, v34, v35
	v_cvt_pk_f16_f32 v187, v36, v37
	v_cvt_pk_f16_f32 v180, v46, v47
	v_cvt_pk_f16_f32 v181, v48, v49
	v_cvt_pk_f16_f32 v182, v42, v43
	v_cvt_pk_f16_f32 v183, v44, v45
	v_mov_b32_dpp v188, v184 row_ror:8 row_mask:0xf bank_mask:0xf
	v_mov_b32_dpp v189, v185 row_ror:8 row_mask:0xf bank_mask:0xf
	v_mov_b32_dpp v190, v186 row_ror:8 row_mask:0xf bank_mask:0xf
	v_mov_b32_dpp v191, v187 row_ror:8 row_mask:0xf bank_mask:0xf
	v_cndmask_b32_e64 v192, v180, v188, s[22:23]
	v_cndmask_b32_e64 v193, v181, v189, s[22:23]
	v_cndmask_b32_e64 v194, v182, v190, s[22:23]
	v_cndmask_b32_e64 v195, v183, v191, s[22:23]
	v_cndmask_b32_e64 v196, v188, v180, s[22:23]
	v_cndmask_b32_e64 v197, v189, v181, s[22:23]
	v_cndmask_b32_e64 v198, v190, v182, s[22:23]
	v_cndmask_b32_e64 v199, v191, v183, s[22:23]
	global_store_dwordx4 v[172:173], v[192:195], off
	global_store_dwordx4 v[174:175], v[196:199], off
	v_lshl_add_u64 v[172:173], v[172:173], 0, v[178:179]
	v_lshl_add_u64 v[174:175], v[174:175], 0, v[178:179]
	v_mul_f32_e32 v30, v176, v30
	v_mul_f32_e32 v31, v176, v31
	v_mul_f32_e32 v32, v176, v32
	v_mul_f32_e32 v33, v176, v33
	v_mul_f32_e32 v26, v176, v26
	v_mul_f32_e32 v27, v176, v27
	v_mul_f32_e32 v28, v176, v28
	v_mul_f32_e32 v29, v176, v29
	v_mul_f32_e32 v22, v176, v22
	v_mul_f32_e32 v23, v176, v23
	v_mul_f32_e32 v24, v176, v24
	v_mul_f32_e32 v25, v176, v25
	v_mul_f32_e32 v18, v176, v18
	v_mul_f32_e32 v19, v176, v19
	v_mul_f32_e32 v20, v176, v20
	v_mul_f32_e32 v21, v176, v21
	v_cvt_pk_f16_f32 v184, v22, v23
	v_cvt_pk_f16_f32 v185, v24, v25
	v_cvt_pk_f16_f32 v186, v18, v19
	v_cvt_pk_f16_f32 v187, v20, v21
	v_cvt_pk_f16_f32 v180, v30, v31
	v_cvt_pk_f16_f32 v181, v32, v33
	v_cvt_pk_f16_f32 v182, v26, v27
	v_cvt_pk_f16_f32 v183, v28, v29
	v_mov_b32_dpp v188, v184 row_ror:8 row_mask:0xf bank_mask:0xf
	v_mov_b32_dpp v189, v185 row_ror:8 row_mask:0xf bank_mask:0xf
	v_mov_b32_dpp v190, v186 row_ror:8 row_mask:0xf bank_mask:0xf
	v_mov_b32_dpp v191, v187 row_ror:8 row_mask:0xf bank_mask:0xf
	v_cndmask_b32_e64 v192, v180, v188, s[22:23]
	v_cndmask_b32_e64 v193, v181, v189, s[22:23]
	v_cndmask_b32_e64 v194, v182, v190, s[22:23]
	v_cndmask_b32_e64 v195, v183, v191, s[22:23]
	v_cndmask_b32_e64 v196, v188, v180, s[22:23]
	v_cndmask_b32_e64 v197, v189, v181, s[22:23]
	v_cndmask_b32_e64 v198, v190, v182, s[22:23]
	v_cndmask_b32_e64 v199, v191, v183, s[22:23]
	global_store_dwordx4 v[172:173], v[192:195], off
	global_store_dwordx4 v[174:175], v[196:199], off
	v_lshl_add_u64 v[172:173], v[172:173], 0, v[178:179]
	v_lshl_add_u64 v[174:175], v[174:175], 0, v[178:179]
	v_mul_f32_e32 v14, v176, v14
	v_mul_f32_e32 v15, v176, v15
	v_mul_f32_e32 v16, v176, v16
	v_mul_f32_e32 v17, v176, v17
	v_mul_f32_e32 v10, v176, v10
	v_mul_f32_e32 v11, v176, v11
	v_mul_f32_e32 v12, v176, v12
	v_mul_f32_e32 v13, v176, v13
	v_mul_f32_e32 v6, v176, v6
	v_mul_f32_e32 v7, v176, v7
	v_mul_f32_e32 v8, v176, v8
	v_mul_f32_e32 v9, v176, v9
	v_mul_f32_e32 v2, v176, v2
	v_mul_f32_e32 v3, v176, v3
	v_mul_f32_e32 v4, v176, v4
	v_mul_f32_e32 v5, v176, v5
	v_cvt_pk_f16_f32 v184, v6, v7
	v_cvt_pk_f16_f32 v185, v8, v9
	v_cvt_pk_f16_f32 v186, v2, v3
	v_cvt_pk_f16_f32 v187, v4, v5
	v_cvt_pk_f16_f32 v180, v14, v15
	v_cvt_pk_f16_f32 v181, v16, v17
	v_cvt_pk_f16_f32 v182, v10, v11
	v_cvt_pk_f16_f32 v183, v12, v13
	v_mov_b32_dpp v188, v184 row_ror:8 row_mask:0xf bank_mask:0xf
	v_mov_b32_dpp v189, v185 row_ror:8 row_mask:0xf bank_mask:0xf
	v_mov_b32_dpp v190, v186 row_ror:8 row_mask:0xf bank_mask:0xf
	v_mov_b32_dpp v191, v187 row_ror:8 row_mask:0xf bank_mask:0xf
	v_cndmask_b32_e64 v192, v180, v188, s[22:23]
	v_cndmask_b32_e64 v193, v181, v189, s[22:23]
	v_cndmask_b32_e64 v194, v182, v190, s[22:23]
	v_cndmask_b32_e64 v195, v183, v191, s[22:23]
	v_cndmask_b32_e64 v196, v188, v180, s[22:23]
	v_cndmask_b32_e64 v197, v189, v181, s[22:23]
	v_cndmask_b32_e64 v198, v190, v182, s[22:23]
	v_cndmask_b32_e64 v199, v191, v183, s[22:23]
	global_store_dwordx4 v[172:173], v[192:195], off
	global_store_dwordx4 v[174:175], v[196:199], off
	s_branch .Lp2e0_done
.Lp2e0_sig:
	v_mul_f32_e32 v126, 0xbfb8aa3b, v126
	v_mul_f32_e32 v127, 0xbfb8aa3b, v127
	v_mul_f32_e32 v128, 0xbfb8aa3b, v128
	v_mul_f32_e32 v129, 0xbfb8aa3b, v129
	v_mul_f32_e32 v122, 0xbfb8aa3b, v122
	v_mul_f32_e32 v123, 0xbfb8aa3b, v123
	v_mul_f32_e32 v124, 0xbfb8aa3b, v124
	v_mul_f32_e32 v125, 0xbfb8aa3b, v125
	v_mul_f32_e32 v118, 0xbfb8aa3b, v118
	v_mul_f32_e32 v119, 0xbfb8aa3b, v119
	v_mul_f32_e32 v120, 0xbfb8aa3b, v120
	v_mul_f32_e32 v121, 0xbfb8aa3b, v121
	v_mul_f32_e32 v114, 0xbfb8aa3b, v114
	v_mul_f32_e32 v115, 0xbfb8aa3b, v115
	v_mul_f32_e32 v116, 0xbfb8aa3b, v116
	v_mul_f32_e32 v117, 0xbfb8aa3b, v117
	v_exp_f32_e32 v126, v126
	v_exp_f32_e32 v127, v127
	v_exp_f32_e32 v128, v128
	v_exp_f32_e32 v129, v129
	v_exp_f32_e32 v122, v122
	v_exp_f32_e32 v123, v123
	v_exp_f32_e32 v124, v124
	v_exp_f32_e32 v125, v125
	v_exp_f32_e32 v118, v118
	v_exp_f32_e32 v119, v119
	v_exp_f32_e32 v120, v120
	v_exp_f32_e32 v121, v121
	v_exp_f32_e32 v114, v114
	v_exp_f32_e32 v115, v115
	v_exp_f32_e32 v116, v116
	v_exp_f32_e32 v117, v117
	v_add_f32_e32 v126, 1.0, v126
	v_add_f32_e32 v127, 1.0, v127
	v_add_f32_e32 v128, 1.0, v128
	v_add_f32_e32 v129, 1.0, v129
	v_add_f32_e32 v122, 1.0, v122
	v_add_f32_e32 v123, 1.0, v123
	v_add_f32_e32 v124, 1.0, v124
	v_add_f32_e32 v125, 1.0, v125
	v_add_f32_e32 v118, 1.0, v118
	v_add_f32_e32 v119, 1.0, v119
	v_add_f32_e32 v120, 1.0, v120
	v_add_f32_e32 v121, 1.0, v121
	v_add_f32_e32 v114, 1.0, v114
	v_add_f32_e32 v115, 1.0, v115
	v_add_f32_e32 v116, 1.0, v116
	v_add_f32_e32 v117, 1.0, v117
	v_rcp_f32_e32 v126, v126
	v_rcp_f32_e32 v127, v127
	v_rcp_f32_e32 v128, v128
	v_rcp_f32_e32 v129, v129
	v_rcp_f32_e32 v122, v122
	v_rcp_f32_e32 v123, v123
	v_rcp_f32_e32 v124, v124
	v_rcp_f32_e32 v125, v125
	v_rcp_f32_e32 v118, v118
	v_rcp_f32_e32 v119, v119
	v_rcp_f32_e32 v120, v120
	v_rcp_f32_e32 v121, v121
	v_rcp_f32_e32 v114, v114
	v_rcp_f32_e32 v115, v115
	v_rcp_f32_e32 v116, v116
	v_rcp_f32_e32 v117, v117
	v_cvt_pk_f16_f32 v184, v118, v119
	v_cvt_pk_f16_f32 v185, v120, v121
	v_cvt_pk_f16_f32 v186, v114, v115
	v_cvt_pk_f16_f32 v187, v116, v117
	v_cvt_pk_f16_f32 v180, v126, v127
	v_cvt_pk_f16_f32 v181, v128, v129
	v_cvt_pk_f16_f32 v182, v122, v123
	v_cvt_pk_f16_f32 v183, v124, v125
	v_mov_b32_dpp v188, v184 row_ror:8 row_mask:0xf bank_mask:0xf
	v_mov_b32_dpp v189, v185 row_ror:8 row_mask:0xf bank_mask:0xf
	v_mov_b32_dpp v190, v186 row_ror:8 row_mask:0xf bank_mask:0xf
	v_mov_b32_dpp v191, v187 row_ror:8 row_mask:0xf bank_mask:0xf
	v_cndmask_b32_e64 v192, v180, v188, s[22:23]
	v_cndmask_b32_e64 v193, v181, v189, s[22:23]
	v_cndmask_b32_e64 v194, v182, v190, s[22:23]
	v_cndmask_b32_e64 v195, v183, v191, s[22:23]
	v_cndmask_b32_e64 v196, v188, v180, s[22:23]
	v_cndmask_b32_e64 v197, v189, v181, s[22:23]
	v_cndmask_b32_e64 v198, v190, v182, s[22:23]
	v_cndmask_b32_e64 v199, v191, v183, s[22:23]
	global_store_dwordx4 v[172:173], v[192:195], off
	global_store_dwordx4 v[174:175], v[196:199], off
	v_lshl_add_u64 v[172:173], v[172:173], 0, v[178:179]
	v_lshl_add_u64 v[174:175], v[174:175], 0, v[178:179]
	v_mul_f32_e32 v110, 0xbfb8aa3b, v110
	v_mul_f32_e32 v111, 0xbfb8aa3b, v111
	v_mul_f32_e32 v112, 0xbfb8aa3b, v112
	v_mul_f32_e32 v113, 0xbfb8aa3b, v113
	v_mul_f32_e32 v106, 0xbfb8aa3b, v106
	v_mul_f32_e32 v107, 0xbfb8aa3b, v107
	v_mul_f32_e32 v108, 0xbfb8aa3b, v108
	v_mul_f32_e32 v109, 0xbfb8aa3b, v109
	v_mul_f32_e32 v102, 0xbfb8aa3b, v102
	v_mul_f32_e32 v103, 0xbfb8aa3b, v103
	v_mul_f32_e32 v104, 0xbfb8aa3b, v104
	v_mul_f32_e32 v105, 0xbfb8aa3b, v105
	v_mul_f32_e32 v98, 0xbfb8aa3b, v98
	v_mul_f32_e32 v99, 0xbfb8aa3b, v99
	v_mul_f32_e32 v100, 0xbfb8aa3b, v100
	v_mul_f32_e32 v101, 0xbfb8aa3b, v101
	v_exp_f32_e32 v110, v110
	v_exp_f32_e32 v111, v111
	v_exp_f32_e32 v112, v112
	v_exp_f32_e32 v113, v113
	v_exp_f32_e32 v106, v106
	v_exp_f32_e32 v107, v107
	v_exp_f32_e32 v108, v108
	v_exp_f32_e32 v109, v109
	v_exp_f32_e32 v102, v102
	v_exp_f32_e32 v103, v103
	v_exp_f32_e32 v104, v104
	v_exp_f32_e32 v105, v105
	v_exp_f32_e32 v98, v98
	v_exp_f32_e32 v99, v99
	v_exp_f32_e32 v100, v100
	v_exp_f32_e32 v101, v101
	v_add_f32_e32 v110, 1.0, v110
	v_add_f32_e32 v111, 1.0, v111
	v_add_f32_e32 v112, 1.0, v112
	v_add_f32_e32 v113, 1.0, v113
	v_add_f32_e32 v106, 1.0, v106
	v_add_f32_e32 v107, 1.0, v107
	v_add_f32_e32 v108, 1.0, v108
	v_add_f32_e32 v109, 1.0, v109
	v_add_f32_e32 v102, 1.0, v102
	v_add_f32_e32 v103, 1.0, v103
	v_add_f32_e32 v104, 1.0, v104
	v_add_f32_e32 v105, 1.0, v105
	v_add_f32_e32 v98, 1.0, v98
	v_add_f32_e32 v99, 1.0, v99
	v_add_f32_e32 v100, 1.0, v100
	v_add_f32_e32 v101, 1.0, v101
	v_rcp_f32_e32 v110, v110
	v_rcp_f32_e32 v111, v111
	v_rcp_f32_e32 v112, v112
	v_rcp_f32_e32 v113, v113
	v_rcp_f32_e32 v106, v106
	v_rcp_f32_e32 v107, v107
	v_rcp_f32_e32 v108, v108
	v_rcp_f32_e32 v109, v109
	v_rcp_f32_e32 v102, v102
	v_rcp_f32_e32 v103, v103
	v_rcp_f32_e32 v104, v104
	v_rcp_f32_e32 v105, v105
	v_rcp_f32_e32 v98, v98
	v_rcp_f32_e32 v99, v99
	v_rcp_f32_e32 v100, v100
	v_rcp_f32_e32 v101, v101
	v_cvt_pk_f16_f32 v184, v102, v103
	v_cvt_pk_f16_f32 v185, v104, v105
	v_cvt_pk_f16_f32 v186, v98, v99
	v_cvt_pk_f16_f32 v187, v100, v101
	v_cvt_pk_f16_f32 v180, v110, v111
	v_cvt_pk_f16_f32 v181, v112, v113
	v_cvt_pk_f16_f32 v182, v106, v107
	v_cvt_pk_f16_f32 v183, v108, v109
	v_mov_b32_dpp v188, v184 row_ror:8 row_mask:0xf bank_mask:0xf
	v_mov_b32_dpp v189, v185 row_ror:8 row_mask:0xf bank_mask:0xf
	v_mov_b32_dpp v190, v186 row_ror:8 row_mask:0xf bank_mask:0xf
	v_mov_b32_dpp v191, v187 row_ror:8 row_mask:0xf bank_mask:0xf
	v_cndmask_b32_e64 v192, v180, v188, s[22:23]
	v_cndmask_b32_e64 v193, v181, v189, s[22:23]
	v_cndmask_b32_e64 v194, v182, v190, s[22:23]
	v_cndmask_b32_e64 v195, v183, v191, s[22:23]
	v_cndmask_b32_e64 v196, v188, v180, s[22:23]
	v_cndmask_b32_e64 v197, v189, v181, s[22:23]
	v_cndmask_b32_e64 v198, v190, v182, s[22:23]
	v_cndmask_b32_e64 v199, v191, v183, s[22:23]
	global_store_dwordx4 v[172:173], v[192:195], off
	global_store_dwordx4 v[174:175], v[196:199], off
	v_lshl_add_u64 v[172:173], v[172:173], 0, v[178:179]
	v_lshl_add_u64 v[174:175], v[174:175], 0, v[178:179]
	v_mul_f32_e32 v94, 0xbfb8aa3b, v94
	v_mul_f32_e32 v95, 0xbfb8aa3b, v95
	v_mul_f32_e32 v96, 0xbfb8aa3b, v96
	v_mul_f32_e32 v97, 0xbfb8aa3b, v97
	v_mul_f32_e32 v90, 0xbfb8aa3b, v90
	v_mul_f32_e32 v91, 0xbfb8aa3b, v91
	v_mul_f32_e32 v92, 0xbfb8aa3b, v92
	v_mul_f32_e32 v93, 0xbfb8aa3b, v93
	v_mul_f32_e32 v86, 0xbfb8aa3b, v86
	v_mul_f32_e32 v87, 0xbfb8aa3b, v87
	v_mul_f32_e32 v88, 0xbfb8aa3b, v88
	v_mul_f32_e32 v89, 0xbfb8aa3b, v89
	v_mul_f32_e32 v82, 0xbfb8aa3b, v82
	v_mul_f32_e32 v83, 0xbfb8aa3b, v83
	v_mul_f32_e32 v84, 0xbfb8aa3b, v84
	v_mul_f32_e32 v85, 0xbfb8aa3b, v85
	v_exp_f32_e32 v94, v94
	v_exp_f32_e32 v95, v95
	v_exp_f32_e32 v96, v96
	v_exp_f32_e32 v97, v97
	v_exp_f32_e32 v90, v90
	v_exp_f32_e32 v91, v91
	v_exp_f32_e32 v92, v92
	v_exp_f32_e32 v93, v93
	v_exp_f32_e32 v86, v86
	v_exp_f32_e32 v87, v87
	v_exp_f32_e32 v88, v88
	v_exp_f32_e32 v89, v89
	v_exp_f32_e32 v82, v82
	v_exp_f32_e32 v83, v83
	v_exp_f32_e32 v84, v84
	v_exp_f32_e32 v85, v85
	v_add_f32_e32 v94, 1.0, v94
	v_add_f32_e32 v95, 1.0, v95
	v_add_f32_e32 v96, 1.0, v96
	v_add_f32_e32 v97, 1.0, v97
	v_add_f32_e32 v90, 1.0, v90
	v_add_f32_e32 v91, 1.0, v91
	v_add_f32_e32 v92, 1.0, v92
	v_add_f32_e32 v93, 1.0, v93
	v_add_f32_e32 v86, 1.0, v86
	v_add_f32_e32 v87, 1.0, v87
	v_add_f32_e32 v88, 1.0, v88
	v_add_f32_e32 v89, 1.0, v89
	v_add_f32_e32 v82, 1.0, v82
	v_add_f32_e32 v83, 1.0, v83
	v_add_f32_e32 v84, 1.0, v84
	v_add_f32_e32 v85, 1.0, v85
	v_rcp_f32_e32 v94, v94
	v_rcp_f32_e32 v95, v95
	v_rcp_f32_e32 v96, v96
	v_rcp_f32_e32 v97, v97
	v_rcp_f32_e32 v90, v90
	v_rcp_f32_e32 v91, v91
	v_rcp_f32_e32 v92, v92
	v_rcp_f32_e32 v93, v93
	v_rcp_f32_e32 v86, v86
	v_rcp_f32_e32 v87, v87
	v_rcp_f32_e32 v88, v88
	v_rcp_f32_e32 v89, v89
	v_rcp_f32_e32 v82, v82
	v_rcp_f32_e32 v83, v83
	v_rcp_f32_e32 v84, v84
	v_rcp_f32_e32 v85, v85
	v_cvt_pk_f16_f32 v184, v86, v87
	v_cvt_pk_f16_f32 v185, v88, v89
	v_cvt_pk_f16_f32 v186, v82, v83
	v_cvt_pk_f16_f32 v187, v84, v85
	v_cvt_pk_f16_f32 v180, v94, v95
	v_cvt_pk_f16_f32 v181, v96, v97
	v_cvt_pk_f16_f32 v182, v90, v91
	v_cvt_pk_f16_f32 v183, v92, v93
	v_mov_b32_dpp v188, v184 row_ror:8 row_mask:0xf bank_mask:0xf
	v_mov_b32_dpp v189, v185 row_ror:8 row_mask:0xf bank_mask:0xf
	v_mov_b32_dpp v190, v186 row_ror:8 row_mask:0xf bank_mask:0xf
	v_mov_b32_dpp v191, v187 row_ror:8 row_mask:0xf bank_mask:0xf
	v_cndmask_b32_e64 v192, v180, v188, s[22:23]
	v_cndmask_b32_e64 v193, v181, v189, s[22:23]
	v_cndmask_b32_e64 v194, v182, v190, s[22:23]
	v_cndmask_b32_e64 v195, v183, v191, s[22:23]
	v_cndmask_b32_e64 v196, v188, v180, s[22:23]
	v_cndmask_b32_e64 v197, v189, v181, s[22:23]
	v_cndmask_b32_e64 v198, v190, v182, s[22:23]
	v_cndmask_b32_e64 v199, v191, v183, s[22:23]
	global_store_dwordx4 v[172:173], v[192:195], off
	global_store_dwordx4 v[174:175], v[196:199], off
	v_lshl_add_u64 v[172:173], v[172:173], 0, v[178:179]
	v_lshl_add_u64 v[174:175], v[174:175], 0, v[178:179]
	v_mul_f32_e32 v78, 0xbfb8aa3b, v78
	v_mul_f32_e32 v79, 0xbfb8aa3b, v79
	v_mul_f32_e32 v80, 0xbfb8aa3b, v80
	v_mul_f32_e32 v81, 0xbfb8aa3b, v81
	v_mul_f32_e32 v74, 0xbfb8aa3b, v74
	v_mul_f32_e32 v75, 0xbfb8aa3b, v75
	v_mul_f32_e32 v76, 0xbfb8aa3b, v76
	v_mul_f32_e32 v77, 0xbfb8aa3b, v77
	v_mul_f32_e32 v70, 0xbfb8aa3b, v70
	v_mul_f32_e32 v71, 0xbfb8aa3b, v71
	v_mul_f32_e32 v72, 0xbfb8aa3b, v72
	v_mul_f32_e32 v73, 0xbfb8aa3b, v73
	v_mul_f32_e32 v66, 0xbfb8aa3b, v66
	v_mul_f32_e32 v67, 0xbfb8aa3b, v67
	v_mul_f32_e32 v68, 0xbfb8aa3b, v68
	v_mul_f32_e32 v69, 0xbfb8aa3b, v69
	v_exp_f32_e32 v78, v78
	v_exp_f32_e32 v79, v79
	v_exp_f32_e32 v80, v80
	v_exp_f32_e32 v81, v81
	v_exp_f32_e32 v74, v74
	v_exp_f32_e32 v75, v75
	v_exp_f32_e32 v76, v76
	v_exp_f32_e32 v77, v77
	v_exp_f32_e32 v70, v70
	v_exp_f32_e32 v71, v71
	v_exp_f32_e32 v72, v72
	v_exp_f32_e32 v73, v73
	v_exp_f32_e32 v66, v66
	v_exp_f32_e32 v67, v67
	v_exp_f32_e32 v68, v68
	v_exp_f32_e32 v69, v69
	v_add_f32_e32 v78, 1.0, v78
	v_add_f32_e32 v79, 1.0, v79
	v_add_f32_e32 v80, 1.0, v80
	v_add_f32_e32 v81, 1.0, v81
	v_add_f32_e32 v74, 1.0, v74
	v_add_f32_e32 v75, 1.0, v75
	v_add_f32_e32 v76, 1.0, v76
	v_add_f32_e32 v77, 1.0, v77
	v_add_f32_e32 v70, 1.0, v70
	v_add_f32_e32 v71, 1.0, v71
	v_add_f32_e32 v72, 1.0, v72
	v_add_f32_e32 v73, 1.0, v73
	v_add_f32_e32 v66, 1.0, v66
	v_add_f32_e32 v67, 1.0, v67
	v_add_f32_e32 v68, 1.0, v68
	v_add_f32_e32 v69, 1.0, v69
	v_rcp_f32_e32 v78, v78
	v_rcp_f32_e32 v79, v79
	v_rcp_f32_e32 v80, v80
	v_rcp_f32_e32 v81, v81
	v_rcp_f32_e32 v74, v74
	v_rcp_f32_e32 v75, v75
	v_rcp_f32_e32 v76, v76
	v_rcp_f32_e32 v77, v77
	v_rcp_f32_e32 v70, v70
	v_rcp_f32_e32 v71, v71
	v_rcp_f32_e32 v72, v72
	v_rcp_f32_e32 v73, v73
	v_rcp_f32_e32 v66, v66
	v_rcp_f32_e32 v67, v67
	v_rcp_f32_e32 v68, v68
	v_rcp_f32_e32 v69, v69
	v_cvt_pk_f16_f32 v184, v70, v71
	v_cvt_pk_f16_f32 v185, v72, v73
	v_cvt_pk_f16_f32 v186, v66, v67
	v_cvt_pk_f16_f32 v187, v68, v69
	v_cvt_pk_f16_f32 v180, v78, v79
	v_cvt_pk_f16_f32 v181, v80, v81
	v_cvt_pk_f16_f32 v182, v74, v75
	v_cvt_pk_f16_f32 v183, v76, v77
	v_mov_b32_dpp v188, v184 row_ror:8 row_mask:0xf bank_mask:0xf
	v_mov_b32_dpp v189, v185 row_ror:8 row_mask:0xf bank_mask:0xf
	v_mov_b32_dpp v190, v186 row_ror:8 row_mask:0xf bank_mask:0xf
	v_mov_b32_dpp v191, v187 row_ror:8 row_mask:0xf bank_mask:0xf
	v_cndmask_b32_e64 v192, v180, v188, s[22:23]
	v_cndmask_b32_e64 v193, v181, v189, s[22:23]
	v_cndmask_b32_e64 v194, v182, v190, s[22:23]
	v_cndmask_b32_e64 v195, v183, v191, s[22:23]
	v_cndmask_b32_e64 v196, v188, v180, s[22:23]
	v_cndmask_b32_e64 v197, v189, v181, s[22:23]
	v_cndmask_b32_e64 v198, v190, v182, s[22:23]
	v_cndmask_b32_e64 v199, v191, v183, s[22:23]
	global_store_dwordx4 v[172:173], v[192:195], off
	global_store_dwordx4 v[174:175], v[196:199], off
	v_lshl_add_u64 v[172:173], v[172:173], 0, v[200:201]
	v_lshl_add_u64 v[174:175], v[174:175], 0, v[200:201]
	v_mul_f32_e32 v62, 0xbfb8aa3b, v62
	v_mul_f32_e32 v63, 0xbfb8aa3b, v63
	v_mul_f32_e32 v64, 0xbfb8aa3b, v64
	v_mul_f32_e32 v65, 0xbfb8aa3b, v65
	v_mul_f32_e32 v58, 0xbfb8aa3b, v58
	v_mul_f32_e32 v59, 0xbfb8aa3b, v59
	v_mul_f32_e32 v60, 0xbfb8aa3b, v60
	v_mul_f32_e32 v61, 0xbfb8aa3b, v61
	v_mul_f32_e32 v54, 0xbfb8aa3b, v54
	v_mul_f32_e32 v55, 0xbfb8aa3b, v55
	v_mul_f32_e32 v56, 0xbfb8aa3b, v56
	v_mul_f32_e32 v57, 0xbfb8aa3b, v57
	v_mul_f32_e32 v50, 0xbfb8aa3b, v50
	v_mul_f32_e32 v51, 0xbfb8aa3b, v51
	v_mul_f32_e32 v52, 0xbfb8aa3b, v52
	v_mul_f32_e32 v53, 0xbfb8aa3b, v53
	v_exp_f32_e32 v62, v62
	v_exp_f32_e32 v63, v63
	v_exp_f32_e32 v64, v64
	v_exp_f32_e32 v65, v65
	v_exp_f32_e32 v58, v58
	v_exp_f32_e32 v59, v59
	v_exp_f32_e32 v60, v60
	v_exp_f32_e32 v61, v61
	v_exp_f32_e32 v54, v54
	v_exp_f32_e32 v55, v55
	v_exp_f32_e32 v56, v56
	v_exp_f32_e32 v57, v57
	v_exp_f32_e32 v50, v50
	v_exp_f32_e32 v51, v51
	v_exp_f32_e32 v52, v52
	v_exp_f32_e32 v53, v53
	v_add_f32_e32 v62, 1.0, v62
	v_add_f32_e32 v63, 1.0, v63
	v_add_f32_e32 v64, 1.0, v64
	v_add_f32_e32 v65, 1.0, v65
	v_add_f32_e32 v58, 1.0, v58
	v_add_f32_e32 v59, 1.0, v59
	v_add_f32_e32 v60, 1.0, v60
	v_add_f32_e32 v61, 1.0, v61
	v_add_f32_e32 v54, 1.0, v54
	v_add_f32_e32 v55, 1.0, v55
	v_add_f32_e32 v56, 1.0, v56
	v_add_f32_e32 v57, 1.0, v57
	v_add_f32_e32 v50, 1.0, v50
	v_add_f32_e32 v51, 1.0, v51
	v_add_f32_e32 v52, 1.0, v52
	v_add_f32_e32 v53, 1.0, v53
	v_rcp_f32_e32 v62, v62
	v_rcp_f32_e32 v63, v63
	v_rcp_f32_e32 v64, v64
	v_rcp_f32_e32 v65, v65
	v_rcp_f32_e32 v58, v58
	v_rcp_f32_e32 v59, v59
	v_rcp_f32_e32 v60, v60
	v_rcp_f32_e32 v61, v61
	v_rcp_f32_e32 v54, v54
	v_rcp_f32_e32 v55, v55
	v_rcp_f32_e32 v56, v56
	v_rcp_f32_e32 v57, v57
	v_rcp_f32_e32 v50, v50
	v_rcp_f32_e32 v51, v51
	v_rcp_f32_e32 v52, v52
	v_rcp_f32_e32 v53, v53
	v_cvt_pk_f16_f32 v184, v54, v55
	v_cvt_pk_f16_f32 v185, v56, v57
	v_cvt_pk_f16_f32 v186, v50, v51
	v_cvt_pk_f16_f32 v187, v52, v53
	v_cvt_pk_f16_f32 v180, v62, v63
	v_cvt_pk_f16_f32 v181, v64, v65
	v_cvt_pk_f16_f32 v182, v58, v59
	v_cvt_pk_f16_f32 v183, v60, v61
	v_mov_b32_dpp v188, v184 row_ror:8 row_mask:0xf bank_mask:0xf
	v_mov_b32_dpp v189, v185 row_ror:8 row_mask:0xf bank_mask:0xf
	v_mov_b32_dpp v190, v186 row_ror:8 row_mask:0xf bank_mask:0xf
	v_mov_b32_dpp v191, v187 row_ror:8 row_mask:0xf bank_mask:0xf
	v_cndmask_b32_e64 v192, v180, v188, s[22:23]
	v_cndmask_b32_e64 v193, v181, v189, s[22:23]
	v_cndmask_b32_e64 v194, v182, v190, s[22:23]
	v_cndmask_b32_e64 v195, v183, v191, s[22:23]
	v_cndmask_b32_e64 v196, v188, v180, s[22:23]
	v_cndmask_b32_e64 v197, v189, v181, s[22:23]
	v_cndmask_b32_e64 v198, v190, v182, s[22:23]
	v_cndmask_b32_e64 v199, v191, v183, s[22:23]
	global_store_dwordx4 v[172:173], v[192:195], off
	global_store_dwordx4 v[174:175], v[196:199], off
	v_lshl_add_u64 v[172:173], v[172:173], 0, v[178:179]
	v_lshl_add_u64 v[174:175], v[174:175], 0, v[178:179]
	v_mul_f32_e32 v46, 0xbfb8aa3b, v46
	v_mul_f32_e32 v47, 0xbfb8aa3b, v47
	v_mul_f32_e32 v48, 0xbfb8aa3b, v48
	v_mul_f32_e32 v49, 0xbfb8aa3b, v49
	v_mul_f32_e32 v42, 0xbfb8aa3b, v42
	v_mul_f32_e32 v43, 0xbfb8aa3b, v43
	v_mul_f32_e32 v44, 0xbfb8aa3b, v44
	v_mul_f32_e32 v45, 0xbfb8aa3b, v45
	v_mul_f32_e32 v38, 0xbfb8aa3b, v38
	v_mul_f32_e32 v39, 0xbfb8aa3b, v39
	v_mul_f32_e32 v40, 0xbfb8aa3b, v40
	v_mul_f32_e32 v41, 0xbfb8aa3b, v41
	v_mul_f32_e32 v34, 0xbfb8aa3b, v34
	v_mul_f32_e32 v35, 0xbfb8aa3b, v35
	v_mul_f32_e32 v36, 0xbfb8aa3b, v36
	v_mul_f32_e32 v37, 0xbfb8aa3b, v37
	v_exp_f32_e32 v46, v46
	v_exp_f32_e32 v47, v47
	v_exp_f32_e32 v48, v48
	v_exp_f32_e32 v49, v49
	v_exp_f32_e32 v42, v42
	v_exp_f32_e32 v43, v43
	v_exp_f32_e32 v44, v44
	v_exp_f32_e32 v45, v45
	v_exp_f32_e32 v38, v38
	v_exp_f32_e32 v39, v39
	v_exp_f32_e32 v40, v40
	v_exp_f32_e32 v41, v41
	v_exp_f32_e32 v34, v34
	v_exp_f32_e32 v35, v35
	v_exp_f32_e32 v36, v36
	v_exp_f32_e32 v37, v37
	v_add_f32_e32 v46, 1.0, v46
	v_add_f32_e32 v47, 1.0, v47
	v_add_f32_e32 v48, 1.0, v48
	v_add_f32_e32 v49, 1.0, v49
	v_add_f32_e32 v42, 1.0, v42
	v_add_f32_e32 v43, 1.0, v43
	v_add_f32_e32 v44, 1.0, v44
	v_add_f32_e32 v45, 1.0, v45
	v_add_f32_e32 v38, 1.0, v38
	v_add_f32_e32 v39, 1.0, v39
	v_add_f32_e32 v40, 1.0, v40
	v_add_f32_e32 v41, 1.0, v41
	v_add_f32_e32 v34, 1.0, v34
	v_add_f32_e32 v35, 1.0, v35
	v_add_f32_e32 v36, 1.0, v36
	v_add_f32_e32 v37, 1.0, v37
	v_rcp_f32_e32 v46, v46
	v_rcp_f32_e32 v47, v47
	v_rcp_f32_e32 v48, v48
	v_rcp_f32_e32 v49, v49
	v_rcp_f32_e32 v42, v42
	v_rcp_f32_e32 v43, v43
	v_rcp_f32_e32 v44, v44
	v_rcp_f32_e32 v45, v45
	v_rcp_f32_e32 v38, v38
	v_rcp_f32_e32 v39, v39
	v_rcp_f32_e32 v40, v40
	v_rcp_f32_e32 v41, v41
	v_rcp_f32_e32 v34, v34
	v_rcp_f32_e32 v35, v35
	v_rcp_f32_e32 v36, v36
	v_rcp_f32_e32 v37, v37
	v_cvt_pk_f16_f32 v184, v38, v39
	v_cvt_pk_f16_f32 v185, v40, v41
	v_cvt_pk_f16_f32 v186, v34, v35
	v_cvt_pk_f16_f32 v187, v36, v37
	v_cvt_pk_f16_f32 v180, v46, v47
	v_cvt_pk_f16_f32 v181, v48, v49
	v_cvt_pk_f16_f32 v182, v42, v43
	v_cvt_pk_f16_f32 v183, v44, v45
	v_mov_b32_dpp v188, v184 row_ror:8 row_mask:0xf bank_mask:0xf
	v_mov_b32_dpp v189, v185 row_ror:8 row_mask:0xf bank_mask:0xf
	v_mov_b32_dpp v190, v186 row_ror:8 row_mask:0xf bank_mask:0xf
	v_mov_b32_dpp v191, v187 row_ror:8 row_mask:0xf bank_mask:0xf
	v_cndmask_b32_e64 v192, v180, v188, s[22:23]
	v_cndmask_b32_e64 v193, v181, v189, s[22:23]
	v_cndmask_b32_e64 v194, v182, v190, s[22:23]
	v_cndmask_b32_e64 v195, v183, v191, s[22:23]
	v_cndmask_b32_e64 v196, v188, v180, s[22:23]
	v_cndmask_b32_e64 v197, v189, v181, s[22:23]
	v_cndmask_b32_e64 v198, v190, v182, s[22:23]
	v_cndmask_b32_e64 v199, v191, v183, s[22:23]
	global_store_dwordx4 v[172:173], v[192:195], off
	global_store_dwordx4 v[174:175], v[196:199], off
	v_lshl_add_u64 v[172:173], v[172:173], 0, v[178:179]
	v_lshl_add_u64 v[174:175], v[174:175], 0, v[178:179]
	v_mul_f32_e32 v30, 0xbfb8aa3b, v30
	v_mul_f32_e32 v31, 0xbfb8aa3b, v31
	v_mul_f32_e32 v32, 0xbfb8aa3b, v32
	v_mul_f32_e32 v33, 0xbfb8aa3b, v33
	v_mul_f32_e32 v26, 0xbfb8aa3b, v26
	v_mul_f32_e32 v27, 0xbfb8aa3b, v27
	v_mul_f32_e32 v28, 0xbfb8aa3b, v28
	v_mul_f32_e32 v29, 0xbfb8aa3b, v29
	v_mul_f32_e32 v22, 0xbfb8aa3b, v22
	v_mul_f32_e32 v23, 0xbfb8aa3b, v23
	v_mul_f32_e32 v24, 0xbfb8aa3b, v24
	v_mul_f32_e32 v25, 0xbfb8aa3b, v25
	v_mul_f32_e32 v18, 0xbfb8aa3b, v18
	v_mul_f32_e32 v19, 0xbfb8aa3b, v19
	v_mul_f32_e32 v20, 0xbfb8aa3b, v20
	v_mul_f32_e32 v21, 0xbfb8aa3b, v21
	v_exp_f32_e32 v30, v30
	v_exp_f32_e32 v31, v31
	v_exp_f32_e32 v32, v32
	v_exp_f32_e32 v33, v33
	v_exp_f32_e32 v26, v26
	v_exp_f32_e32 v27, v27
	v_exp_f32_e32 v28, v28
	v_exp_f32_e32 v29, v29
	v_exp_f32_e32 v22, v22
	v_exp_f32_e32 v23, v23
	v_exp_f32_e32 v24, v24
	v_exp_f32_e32 v25, v25
	v_exp_f32_e32 v18, v18
	v_exp_f32_e32 v19, v19
	v_exp_f32_e32 v20, v20
	v_exp_f32_e32 v21, v21
	v_add_f32_e32 v30, 1.0, v30
	v_add_f32_e32 v31, 1.0, v31
	v_add_f32_e32 v32, 1.0, v32
	v_add_f32_e32 v33, 1.0, v33
	v_add_f32_e32 v26, 1.0, v26
	v_add_f32_e32 v27, 1.0, v27
	v_add_f32_e32 v28, 1.0, v28
	v_add_f32_e32 v29, 1.0, v29
	v_add_f32_e32 v22, 1.0, v22
	v_add_f32_e32 v23, 1.0, v23
	v_add_f32_e32 v24, 1.0, v24
	v_add_f32_e32 v25, 1.0, v25
	v_add_f32_e32 v18, 1.0, v18
	v_add_f32_e32 v19, 1.0, v19
	v_add_f32_e32 v20, 1.0, v20
	v_add_f32_e32 v21, 1.0, v21
	v_rcp_f32_e32 v30, v30
	v_rcp_f32_e32 v31, v31
	v_rcp_f32_e32 v32, v32
	v_rcp_f32_e32 v33, v33
	v_rcp_f32_e32 v26, v26
	v_rcp_f32_e32 v27, v27
	v_rcp_f32_e32 v28, v28
	v_rcp_f32_e32 v29, v29
	v_rcp_f32_e32 v22, v22
	v_rcp_f32_e32 v23, v23
	v_rcp_f32_e32 v24, v24
	v_rcp_f32_e32 v25, v25
	v_rcp_f32_e32 v18, v18
	v_rcp_f32_e32 v19, v19
	v_rcp_f32_e32 v20, v20
	v_rcp_f32_e32 v21, v21
	v_cvt_pk_f16_f32 v184, v22, v23
	v_cvt_pk_f16_f32 v185, v24, v25
	v_cvt_pk_f16_f32 v186, v18, v19
	v_cvt_pk_f16_f32 v187, v20, v21
	v_cvt_pk_f16_f32 v180, v30, v31
	v_cvt_pk_f16_f32 v181, v32, v33
	v_cvt_pk_f16_f32 v182, v26, v27
	v_cvt_pk_f16_f32 v183, v28, v29
	v_mov_b32_dpp v188, v184 row_ror:8 row_mask:0xf bank_mask:0xf
	v_mov_b32_dpp v189, v185 row_ror:8 row_mask:0xf bank_mask:0xf
	v_mov_b32_dpp v190, v186 row_ror:8 row_mask:0xf bank_mask:0xf
	v_mov_b32_dpp v191, v187 row_ror:8 row_mask:0xf bank_mask:0xf
	v_cndmask_b32_e64 v192, v180, v188, s[22:23]
	v_cndmask_b32_e64 v193, v181, v189, s[22:23]
	v_cndmask_b32_e64 v194, v182, v190, s[22:23]
	v_cndmask_b32_e64 v195, v183, v191, s[22:23]
	v_cndmask_b32_e64 v196, v188, v180, s[22:23]
	v_cndmask_b32_e64 v197, v189, v181, s[22:23]
	v_cndmask_b32_e64 v198, v190, v182, s[22:23]
	v_cndmask_b32_e64 v199, v191, v183, s[22:23]
	global_store_dwordx4 v[172:173], v[192:195], off
	global_store_dwordx4 v[174:175], v[196:199], off
	v_lshl_add_u64 v[172:173], v[172:173], 0, v[178:179]
	v_lshl_add_u64 v[174:175], v[174:175], 0, v[178:179]
	v_mul_f32_e32 v14, 0xbfb8aa3b, v14
	v_mul_f32_e32 v15, 0xbfb8aa3b, v15
	v_mul_f32_e32 v16, 0xbfb8aa3b, v16
	v_mul_f32_e32 v17, 0xbfb8aa3b, v17
	v_mul_f32_e32 v10, 0xbfb8aa3b, v10
	v_mul_f32_e32 v11, 0xbfb8aa3b, v11
	v_mul_f32_e32 v12, 0xbfb8aa3b, v12
	v_mul_f32_e32 v13, 0xbfb8aa3b, v13
	v_mul_f32_e32 v6, 0xbfb8aa3b, v6
	v_mul_f32_e32 v7, 0xbfb8aa3b, v7
	v_mul_f32_e32 v8, 0xbfb8aa3b, v8
	v_mul_f32_e32 v9, 0xbfb8aa3b, v9
	v_mul_f32_e32 v2, 0xbfb8aa3b, v2
	v_mul_f32_e32 v3, 0xbfb8aa3b, v3
	v_mul_f32_e32 v4, 0xbfb8aa3b, v4
	v_mul_f32_e32 v5, 0xbfb8aa3b, v5
	v_exp_f32_e32 v14, v14
	v_exp_f32_e32 v15, v15
	v_exp_f32_e32 v16, v16
	v_exp_f32_e32 v17, v17
	v_exp_f32_e32 v10, v10
	v_exp_f32_e32 v11, v11
	v_exp_f32_e32 v12, v12
	v_exp_f32_e32 v13, v13
	v_exp_f32_e32 v6, v6
	v_exp_f32_e32 v7, v7
	v_exp_f32_e32 v8, v8
	v_exp_f32_e32 v9, v9
	v_exp_f32_e32 v2, v2
	v_exp_f32_e32 v3, v3
	v_exp_f32_e32 v4, v4
	v_exp_f32_e32 v5, v5
	v_add_f32_e32 v14, 1.0, v14
	v_add_f32_e32 v15, 1.0, v15
	v_add_f32_e32 v16, 1.0, v16
	v_add_f32_e32 v17, 1.0, v17
	v_add_f32_e32 v10, 1.0, v10
	v_add_f32_e32 v11, 1.0, v11
	v_add_f32_e32 v12, 1.0, v12
	v_add_f32_e32 v13, 1.0, v13
	v_add_f32_e32 v6, 1.0, v6
	v_add_f32_e32 v7, 1.0, v7
	v_add_f32_e32 v8, 1.0, v8
	v_add_f32_e32 v9, 1.0, v9
	v_add_f32_e32 v2, 1.0, v2
	v_add_f32_e32 v3, 1.0, v3
	v_add_f32_e32 v4, 1.0, v4
	v_add_f32_e32 v5, 1.0, v5
	v_rcp_f32_e32 v14, v14
	v_rcp_f32_e32 v15, v15
	v_rcp_f32_e32 v16, v16
	v_rcp_f32_e32 v17, v17
	v_rcp_f32_e32 v10, v10
	v_rcp_f32_e32 v11, v11
	v_rcp_f32_e32 v12, v12
	v_rcp_f32_e32 v13, v13
	v_rcp_f32_e32 v6, v6
	v_rcp_f32_e32 v7, v7
	v_rcp_f32_e32 v8, v8
	v_rcp_f32_e32 v9, v9
	v_rcp_f32_e32 v2, v2
	v_rcp_f32_e32 v3, v3
	v_rcp_f32_e32 v4, v4
	v_rcp_f32_e32 v5, v5
	v_cvt_pk_f16_f32 v184, v6, v7
	v_cvt_pk_f16_f32 v185, v8, v9
	v_cvt_pk_f16_f32 v186, v2, v3
	v_cvt_pk_f16_f32 v187, v4, v5
	v_cvt_pk_f16_f32 v180, v14, v15
	v_cvt_pk_f16_f32 v181, v16, v17
	v_cvt_pk_f16_f32 v182, v10, v11
	v_cvt_pk_f16_f32 v183, v12, v13
	v_mov_b32_dpp v188, v184 row_ror:8 row_mask:0xf bank_mask:0xf
	v_mov_b32_dpp v189, v185 row_ror:8 row_mask:0xf bank_mask:0xf
	v_mov_b32_dpp v190, v186 row_ror:8 row_mask:0xf bank_mask:0xf
	v_mov_b32_dpp v191, v187 row_ror:8 row_mask:0xf bank_mask:0xf
	v_cndmask_b32_e64 v192, v180, v188, s[22:23]
	v_cndmask_b32_e64 v193, v181, v189, s[22:23]
	v_cndmask_b32_e64 v194, v182, v190, s[22:23]
	v_cndmask_b32_e64 v195, v183, v191, s[22:23]
	v_cndmask_b32_e64 v196, v188, v180, s[22:23]
	v_cndmask_b32_e64 v197, v189, v181, s[22:23]
	v_cndmask_b32_e64 v198, v190, v182, s[22:23]
	v_cndmask_b32_e64 v199, v191, v183, s[22:23]
	global_store_dwordx4 v[172:173], v[192:195], off
	global_store_dwordx4 v[174:175], v[196:199], off
.Lp2e0_done:
	s_mov_b64 s[0:1], -1
	s_and_b64 vcc, exec, s[16:17]
	s_cbranch_vccz .LBB0_205
.LBB0_295:
	s_and_b64 vcc, exec, s[2:3]
	s_cbranch_vccz .LBB0_204
	s_barrier
	s_branch .LBB0_204

.LBB0_1539:
	v_mov_b32_e32 v3, s30
	ds_read_b64 v[20:21], v3
	s_mul_hi_i32 s0, s34, 0x2aaaaaab
	s_lshr_b32 s14, s0, 31
	s_ashr_i32 s0, s0, 5
	s_add_i32 s0, s0, s14
	s_waitcnt lgkmcnt(0)
	v_readfirstlane_b32 s15, v20
	s_mul_i32 s14, s0, 0xc0
	v_readfirstlane_b32 s16, v21
	v_mov_b32_e32 v20, s15
	s_sub_i32 s15, s34, s14
	s_lshl_b32 s14, s0, 6
	s_lshl_b32 s0, s15, 5
	s_and_b32 s100, s0, 0xffffff00
	s_bfe_u32 s101, s0, 0x10005
	s_lshl_b32 s101, s101, 7
	s_or_b32 s100, s100, s101
	s_bfe_u32 s101, s0, 0x20006
	s_lshl_b32 s101, s101, 5
	s_or_b32 s100, s100, s101
	v_or_b32_e32 v28, s0, v5
	v_mov_b32_e32 v21, s16
	v_ashrrev_i32_e32 v29, 31, v28
	v_cmp_gt_i32_e32 vcc, s31, v28
	v_lshl_add_u64 v[20:21], v[28:29], 2, v[20:21]
	s_mov_b32 s15, 0
	v_cndmask_b32_e64 v8, 64, 0, vcc
	v_lshl_add_u64 v[20:21], v[20:21], 0, v[8:9]
	v_lshl_add_u64 v[20:21], v[20:21], 0, s[12:13]
	v_or_b32_e32 v3, s14, v1
	v_or_b32_e32 v8, s14, v2
	s_mov_b32 s16, 1
	s_mov_b32 s17, 32
.LBB0_1540:
	s_lshl_b32 s36, s16, 1
	s_lshl_b32 s37, s15, 1
	v_or_b32_e32 v22, s36, v3
	v_or_b32_e32 v27, s37, v8
	s_add_i32 s38, s36, 4
	s_add_i32 s39, s37, 4
	s_add_i32 s40, s36, 8
	s_add_i32 s41, s37, 8
	s_add_i32 s42, s36, 12
	s_add_i32 s43, s37, 12
	s_add_i32 s44, s36, 16
	s_add_i32 s45, s37, 16
	s_add_i32 s46, s36, 20
	s_add_i32 s47, s37, 20
	s_add_i32 s48, s36, 24
	s_add_i32 s49, s37, 24
	s_add_i32 s50, s36, 28
	s_add_i32 s51, s37, 28
	v_mad_i64_i32 v[28:29], s[34:35], v27, s33, v[20:21]
	v_mad_i64_i32 v[30:31], s[34:35], v22, s33, v[20:21]
	v_or_b32_e32 v22, s38, v3
	v_or_b32_e32 v27, s39, v8
	v_or_b32_e32 v38, s40, v3
	v_or_b32_e32 v36, s41, v8
	v_or_b32_e32 v42, s42, v3
	v_or_b32_e32 v40, s43, v8
	v_or_b32_e32 v46, s44, v3
	v_or_b32_e32 v44, s45, v8
	v_or_b32_e32 v50, s46, v3
	v_or_b32_e32 v48, s47, v8
	v_or_b32_e32 v54, s48, v3
	v_or_b32_e32 v52, s49, v8
	v_or_b32_e32 v58, s50, v3
	v_or_b32_e32 v56, s51, v8
	v_mad_i64_i32 v[32:33], s[34:35], v27, s33, v[20:21]
	v_mad_i64_i32 v[34:35], s[34:35], v22, s33, v[20:21]
	v_mad_i64_i32 v[36:37], s[34:35], v36, s33, v[20:21]
	v_mad_i64_i32 v[38:39], s[34:35], v38, s33, v[20:21]
	v_mad_i64_i32 v[40:41], s[34:35], v40, s33, v[20:21]
	v_mad_i64_i32 v[42:43], s[34:35], v42, s33, v[20:21]
	v_mad_i64_i32 v[44:45], s[34:35], v44, s33, v[20:21]
	v_mad_i64_i32 v[46:47], s[34:35], v46, s33, v[20:21]
	v_mad_i64_i32 v[48:49], s[34:35], v48, s33, v[20:21]
	v_mad_i64_i32 v[50:51], s[34:35], v50, s33, v[20:21]
	v_mad_i64_i32 v[52:53], s[34:35], v52, s33, v[20:21]
	v_mad_i64_i32 v[54:55], s[34:35], v54, s33, v[20:21]
	v_mad_i64_i32 v[56:57], s[34:35], v56, s33, v[20:21]
	v_mad_i64_i32 v[58:59], s[34:35], v58, s33, v[20:21]
	global_load_dword v22, v[28:29], off
	global_load_dword v27, v[30:31], off
	global_load_dword v60, v[32:33], off
	global_load_dword v61, v[34:35], off
	global_load_dword v62, v[36:37], off
	global_load_dword v63, v[38:39], off
	global_load_dword v64, v[40:41], off
	global_load_dword v65, v[42:43], off
	global_load_dword v66, v[44:45], off
	global_load_dword v67, v[46:47], off
	global_load_dword v68, v[48:49], off
	global_load_dword v69, v[50:51], off
	global_load_dword v70, v[52:53], off
	global_load_dword v71, v[54:55], off
	global_load_dword v72, v[56:57], off
	global_load_dword v73, v[58:59], off
	v_or_b32_e32 v30, s36, v1
	v_or_b32_e32 v28, s37, v2
	s_add_i32 s15, s15, 16
	s_add_i32 s16, s16, 16
	s_add_i32 s17, s17, -16
	v_mad_u64_u32 v[28:29], s[34:35], v28, s20, v[4:5]
	v_mad_u64_u32 v[30:31], s[34:35], v30, s20, v[4:5]
	v_or_b32_e32 v29, s38, v1
	v_or_b32_e32 v31, s39, v2
	v_or_b32_e32 v38, s40, v1
	v_or_b32_e32 v36, s41, v2
	v_or_b32_e32 v42, s42, v1
	v_or_b32_e32 v40, s43, v2
	v_or_b32_e32 v46, s44, v1
	v_or_b32_e32 v44, s45, v2
	v_or_b32_e32 v50, s46, v1
	v_or_b32_e32 v48, s47, v2
	v_or_b32_e32 v54, s48, v1
	v_or_b32_e32 v52, s49, v2
	v_or_b32_e32 v58, s50, v1
	v_or_b32_e32 v56, s51, v2
	s_cmp_lg_u32 s17, 0
	v_mad_u64_u32 v[32:33], s[34:35], v31, s20, v[4:5]
	v_mad_u64_u32 v[34:35], s[34:35], v29, s20, v[4:5]
	v_mad_u64_u32 v[36:37], s[34:35], v36, s20, v[4:5]
	v_mad_u64_u32 v[38:39], s[34:35], v38, s20, v[4:5]
	v_mad_u64_u32 v[40:41], s[34:35], v40, s20, v[4:5]
	v_mad_u64_u32 v[42:43], s[34:35], v42, s20, v[4:5]
	v_mad_u64_u32 v[44:45], s[34:35], v44, s20, v[4:5]
	v_mad_u64_u32 v[46:47], s[34:35], v46, s20, v[4:5]
	v_mad_u64_u32 v[48:49], s[34:35], v48, s20, v[4:5]
	v_mad_u64_u32 v[50:51], s[34:35], v50, s20, v[4:5]
	v_mad_u64_u32 v[52:53], s[34:35], v52, s20, v[4:5]
	v_mad_u64_u32 v[54:55], s[34:35], v54, s20, v[4:5]
	v_mad_u64_u32 v[56:57], s[34:35], v56, s20, v[4:5]
	v_mad_u64_u32 v[58:59], s[34:35], v58, s20, v[4:5]
	s_waitcnt vmcnt(15)
	ds_write_b32 v28, v22
	s_waitcnt vmcnt(14)
	ds_write_b32 v30, v27
	s_waitcnt vmcnt(13)
	ds_write_b32 v32, v60
	s_waitcnt vmcnt(12)
	ds_write_b32 v34, v61
	s_waitcnt vmcnt(11)
	ds_write_b32 v36, v62
	s_waitcnt vmcnt(10)
	ds_write_b32 v38, v63
	s_waitcnt vmcnt(9)
	ds_write_b32 v40, v64
	s_waitcnt vmcnt(8)
	ds_write_b32 v42, v65
	s_waitcnt vmcnt(7)
	ds_write_b32 v44, v66
	s_waitcnt vmcnt(6)
	ds_write_b32 v46, v67
	s_waitcnt vmcnt(5)
	ds_write_b32 v48, v68
	s_waitcnt vmcnt(4)
	ds_write_b32 v50, v69
	s_waitcnt vmcnt(3)
	ds_write_b32 v52, v70
	s_waitcnt vmcnt(2)
	ds_write_b32 v54, v71
	s_waitcnt vmcnt(1)
	ds_write_b32 v56, v72
	s_waitcnt vmcnt(0)
	ds_write_b32 v58, v73
	s_cbranch_scc1 .LBB0_1540
	s_waitcnt lgkmcnt(0)
	ds_read2_b32 v[20:21], v23 offset0:33 offset1:41
	ds_read2_b32 v[32:33], v23 offset0:66 offset1:74
	ds_read2_b32 v[34:35], v23 offset0:132 offset1:140
	ds_read2_b32 v[36:37], v23 offset0:198 offset1:206
	ds_read2_b32 v[38:39], v23 offset0:231 offset1:239
	ds_read2_b32 v[40:41], v23 offset0:165 offset1:173
	ds_read2_b32 v[42:43], v23 offset0:99 offset1:107
	ds_read2_b32 v[44:45], v23 offset1:8
	v_or_b32_e32 v48, s100, v7
	s_ashr_i32 s15, s14, 31
	v_ashrrev_i32_e32 v49, 31, v48
	v_lshl_add_u64 v[46:47], s[14:15], 1, v[18:19]
	v_lshlrev_b64 v[48:49], 11, v[48:49]
	s_waitcnt lgkmcnt(3)
	v_cvt_pk_f16_f32 v31, v36, v38
	s_waitcnt lgkmcnt(2)
	v_cvt_pk_f16_f32 v30, v34, v40
	s_waitcnt lgkmcnt(1)
	v_cvt_pk_f16_f32 v29, v32, v42
	s_waitcnt lgkmcnt(0)
	v_cvt_pk_f16_f32 v28, v44, v20
	v_lshl_add_u64 v[48:49], v[46:47], 0, v[48:49]
	v_or_b32_e32 v20, s100, v24
	global_store_dwordx4 v[48:49], v[28:31], off
	s_nop 1
	v_cvt_pk_f16_f32 v28, v45, v21
	v_ashrrev_i32_e32 v21, 31, v20
	v_cvt_pk_f16_f32 v31, v37, v39
	v_cvt_pk_f16_f32 v30, v35, v41
	v_cvt_pk_f16_f32 v29, v33, v43
	v_lshlrev_b64 v[20:21], 11, v[20:21]
	ds_read2_b32 v[32:33], v23 offset0:49 offset1:57
	ds_read2_b32 v[34:35], v23 offset0:82 offset1:90
	ds_read2_b32 v[36:37], v23 offset0:148 offset1:156
	ds_read2_b32 v[38:39], v23 offset0:214 offset1:222
	ds_read2_b32 v[40:41], v23 offset0:247 offset1:255
	ds_read2_b32 v[42:43], v23 offset0:181 offset1:189
	ds_read2_b32 v[44:45], v23 offset0:115 offset1:123
	ds_read2_b32 v[48:49], v23 offset0:16 offset1:24
	v_lshl_add_u64 v[20:21], v[46:47], 0, v[20:21]
	global_store_dwordx4 v[20:21], v[28:31], off
	v_or_b32_e32 v20, s100, v25
	v_ashrrev_i32_e32 v21, 31, v20
	v_lshlrev_b64 v[20:21], 11, v[20:21]
	s_waitcnt lgkmcnt(3)
	v_cvt_pk_f16_f32 v31, v38, v40
	s_waitcnt lgkmcnt(2)
	v_cvt_pk_f16_f32 v30, v36, v42
	s_waitcnt lgkmcnt(1)
	v_cvt_pk_f16_f32 v29, v34, v44
	s_waitcnt lgkmcnt(0)
	v_cvt_pk_f16_f32 v28, v48, v32
	v_lshl_add_u64 v[20:21], v[46:47], 0, v[20:21]
	global_store_dwordx4 v[20:21], v[28:31], off
	v_or_b32_e32 v20, s100, v26
	v_ashrrev_i32_e32 v21, 31, v20
	v_lshlrev_b64 v[20:21], 11, v[20:21]
	v_cvt_pk_f16_f32 v31, v39, v41
	v_cvt_pk_f16_f32 v30, v37, v43
	v_cvt_pk_f16_f32 v29, v35, v45
	v_cvt_pk_f16_f32 v28, v49, v33
	v_lshl_add_u64 v[20:21], v[46:47], 0, v[20:21]
	global_store_dwordx4 v[20:21], v[28:31], off
	s_waitcnt lgkmcnt(0)
	s_branch .LBB0_1503

.Lp2e1_done:
	s_mov_b64 s[0:1], -1
	s_and_b64 vcc, exec, s[16:17]
	s_cbranch_vccz .LBB0_1603
.LBB0_1693:
	s_and_b64 vcc, exec, s[2:3]
	s_cbranch_vccz .LBB0_1602
	s_barrier
	s_branch .LBB0_1602

.Lp2e2_done:
	s_mov_b64 s[0:1], -1
	s_and_b64 vcc, exec, s[16:17]
	s_cbranch_vccz .LBB0_3222
.LBB0_3312:
	s_and_b64 vcc, exec, s[2:3]
	s_cbranch_vccz .LBB0_3221
	s_barrier
	s_branch .LBB0_3221

.Lp2e3_done:
	s_mov_b64 s[0:1], -1
	s_and_b64 vcc, exec, s[16:17]
	s_cbranch_vccz .LBB0_4624
.LBB0_4714:
	s_and_b64 vcc, exec, s[2:3]
	s_cbranch_vccz .LBB0_4623
	s_barrier
	s_branch .LBB0_4623
